# P9 main loop: per-segment s_setprio toggles removed, one static priority raise for the second wave half (waves 4-7) for the whole unit loop
# speedup vs baseline: 1.0014x; 1.0014x over previous
.LBB0_1317:
	s_lshl_b64 s[10:11], s[14:15], 12
	s_add_u32 s8, s8, 0x2b500000
	v_lshrrev_b32_e32 v4, 1, v2
	s_addc_u32 s9, s9, 0
	v_and_b32_e32 v4, 24, v4
	s_waitcnt lgkmcnt(0)
	s_add_u32 s10, s16, s10
	v_and_b32_e32 v3, 15, v2
	v_lshlrev_b32_e32 v5, 1, v4
	v_lshlrev_b32_e32 v2, 2, v2
	s_addc_u32 s11, s17, s11
	v_lshl_or_b32 v167, s13, 6, v3
	v_lshl_or_b32 v3, v3, 6, v5
	s_lshl_b32 s1, s13, 13
	v_and_b32_e32 v2, 32, v2
	v_bitop3_b32 v5, v3, s1, v2 bitop3:0xde
	s_lshl_b32 s1, s18, 5
	s_and_b32 s1, s1, 0x60
	s_lshl_b32 s13, s1, 7
	s_add_u32 s18, s28, 0x80
	v_bitop3_b32 v2, v3, s13, v2 bitop3:0xde
	s_waitcnt vmcnt(2)
	s_barrier
	s_addc_u32 s19, s29, 0
	s_add_i32 s14, s44, 0x18000
	s_mov_b32 s13, m0
	s_mov_b32 m0, s14
	s_nop 3
	global_load_lds_dwordx4 v162, s[18:19]
	s_mov_b32 m0, s13
	s_add_i32 s53, s44, 0x1a000
	s_mov_b32 s13, m0
	s_mov_b32 m0, s53
	s_nop 3
	global_load_lds_dwordx4 v164, s[18:19]
	s_mov_b32 m0, s13
	s_add_u32 s18, s36, 0x80
	s_addc_u32 s19, s37, 0
	s_add_i32 s54, s44, 0x8000
	s_mov_b32 s13, m0
	s_mov_b32 m0, s54
	s_nop 3
	global_load_lds_dwordx4 v0, s[18:19]
	s_mov_b32 m0, s13
	s_add_i32 s55, s44, 0xa000
	s_mov_b32 s13, m0
	s_mov_b32 m0, s55
	s_nop 3
	global_load_lds_dwordx4 v163, s[18:19]
	s_mov_b32 m0, s13
	s_add_u32 s18, s28, 0x20080
	s_addc_u32 s19, s29, 0
	s_add_i32 s56, s44, 0x1c000
	s_mov_b32 s13, m0
	s_mov_b32 m0, s56
	s_nop 3
	global_load_lds_dwordx4 v162, s[18:19]
	s_mov_b32 m0, s13
	s_add_i32 s57, s44, 0x1e000
	s_mov_b32 s13, m0
	s_mov_b32 m0, s57
	s_nop 3
	global_load_lds_dwordx4 v164, s[18:19]
	s_mov_b32 m0, s13
	s_add_i32 s58, s44, 0xc000
	s_waitcnt vmcnt(6)
	s_cmpk_lt_u32 s12, 0x100
	s_cselect_b64 s[12:13], -1, 0
	s_cmp_lg_u64 s[16:17], 0
	v_readlane_b32 s18, v252, 22
	s_cselect_b64 s[16:17], -1, 0
	v_or_b32_e32 v168, s1, v4
	s_mov_b32 s59, 0
	v_add_u32_e32 v169, 0, v2
	v_add_u32_e32 v170, 0, v5
	s_mov_b32 s60, s18
	s_barrier
	v_readlane_b32 s19, v252, 23
	s_cmp_ge_u32 s86, 4
	s_cbranch_scc0 .Lp9_noprio
	s_setprio 1
.Lp9_noprio:
	s_branch .LBB0_1320

.LBB0_1323:
	v_add_u32_e32 v2, 0x10000, v169
	v_add_u32_e32 v6, 0x14000, v169
	ds_read_b128 v[26:29], v2
	ds_read_b128 v[30:33], v2 offset:1024
	ds_read_b128 v[18:21], v2 offset:2048
	ds_read_b128 v[22:25], v2 offset:3072
	ds_read_b128 v[10:13], v6
	ds_read_b128 v[14:17], v6 offset:1024
	ds_read_b128 v[2:5], v6 offset:2048
	ds_read_b128 v[6:9], v6 offset:3072
	s_add_u32 s28, s36, 0x100
	s_addc_u32 s29, s37, 0
	s_cmp_eq_u32 s64, 4
	s_cselect_b32 s38, s21, s28
	s_cselect_b32 s39, s1, s29
	s_cselect_b32 s34, s61, s62
	s_cselect_b32 s35, s19, s63
	s_add_u32 s30, s38, 0x80
	s_addc_u32 s31, s39, 0
	ds_read_b128 v[172:175], v170
	ds_read_b128 v[176:179], v170 offset:1024
	ds_read_b128 v[180:183], v170 offset:2048
	ds_read_b128 v[184:187], v170 offset:3072
	ds_read_b128 v[188:191], v170 offset:4096
	ds_read_b128 v[192:195], v170 offset:5120
	ds_read_b128 v[196:199], v170 offset:6144
	ds_read_b128 v[200:203], v170 offset:7168
	s_add_u32 s36, s36, 0x20080
	s_addc_u32 s37, s37, 0
	s_mov_b32 s65, m0
	s_mov_b32 m0, s58
	s_nop 3
	global_load_lds_dwordx4 v0, s[36:37]
	s_mov_b32 m0, s65
	s_add_i32 s65, s44, 0xe000
	s_mov_b32 s66, m0
	s_mov_b32 m0, s65
	s_nop 3
	global_load_lds_dwordx4 v163, s[36:37]
	s_mov_b32 m0, s66
	s_waitcnt vmcnt(8)
	s_waitcnt lgkmcnt(0)
	s_barrier
	s_waitcnt lgkmcnt(6)
	v_mfma_scale_f32_16x16x128_f8f6f4 v[150:153], v[26:33], v[172:179], v[150:153], v165, v166 op_sel_hi:[0,0,0]
	v_mfma_scale_f32_16x16x128_f8f6f4 v[146:149], v[18:25], v[172:179], v[146:149], v165, v166 op_sel_hi:[0,0,0]
	s_waitcnt lgkmcnt(4)
	v_mfma_scale_f32_16x16x128_f8f6f4 v[130:133], v[26:33], v[180:187], v[130:133], v165, v166 op_sel_hi:[0,0,0]
	v_mfma_scale_f32_16x16x128_f8f6f4 v[134:137], v[18:25], v[180:187], v[134:137], v165, v166 op_sel_hi:[0,0,0]
	s_waitcnt lgkmcnt(2)
	v_mfma_scale_f32_16x16x128_f8f6f4 v[106:109], v[26:33], v[188:195], v[106:109], v165, v166 op_sel_hi:[0,0,0]
	v_mfma_scale_f32_16x16x128_f8f6f4 v[110:113], v[18:25], v[188:195], v[110:113], v165, v166 op_sel_hi:[0,0,0]
	s_waitcnt lgkmcnt(0)
	v_mfma_scale_f32_16x16x128_f8f6f4 v[74:77], v[26:33], v[196:203], v[74:77], v165, v166 op_sel_hi:[0,0,0]
	v_mfma_scale_f32_16x16x128_f8f6f4 v[78:81], v[18:25], v[196:203], v[78:81], v165, v166 op_sel_hi:[0,0,0]
	v_mfma_scale_f32_16x16x128_f8f6f4 v[158:161], v[10:17], v[172:179], v[158:161], v165, v166 op_sel_hi:[0,0,0]
	v_mfma_scale_f32_16x16x128_f8f6f4 v[154:157], v[2:9], v[172:179], v[154:157], v165, v166 op_sel_hi:[0,0,0]
	v_mfma_scale_f32_16x16x128_f8f6f4 v[138:141], v[10:17], v[180:187], v[138:141], v165, v166 op_sel_hi:[0,0,0]
	v_mfma_scale_f32_16x16x128_f8f6f4 v[142:145], v[2:9], v[180:187], v[142:145], v165, v166 op_sel_hi:[0,0,0]
	v_mfma_scale_f32_16x16x128_f8f6f4 v[122:125], v[10:17], v[188:195], v[122:125], v165, v166 op_sel_hi:[0,0,0]
	v_mfma_scale_f32_16x16x128_f8f6f4 v[126:129], v[2:9], v[188:195], v[126:129], v165, v166 op_sel_hi:[0,0,0]
	v_mfma_scale_f32_16x16x128_f8f6f4 v[98:101], v[10:17], v[196:203], v[98:101], v165, v166 op_sel_hi:[0,0,0]
	v_mfma_scale_f32_16x16x128_f8f6f4 v[102:105], v[2:9], v[196:203], v[102:105], v165, v166 op_sel_hi:[0,0,0]
	s_barrier
	ds_read_b128 v[172:175], v170 offset:16384
	ds_read_b128 v[176:179], v170 offset:17408
	ds_read_b128 v[180:183], v170 offset:18432
	ds_read_b128 v[184:187], v170 offset:19456
	ds_read_b128 v[188:191], v170 offset:20480
	ds_read_b128 v[192:195], v170 offset:21504
	ds_read_b128 v[196:199], v170 offset:22528
	ds_read_b128 v[200:203], v170 offset:23552
	s_mov_b32 s36, m0
	s_mov_b32 m0, s45
	s_nop 3
	global_load_lds_dwordx4 v162, s[34:35]
	s_mov_b32 m0, s36
	s_nop 0
	s_mov_b32 s36, m0
	s_mov_b32 m0, s47
	s_nop 3
	global_load_lds_dwordx4 v164, s[34:35]
	s_mov_b32 m0, s36
	s_add_u32 s36, s34, 0x20000
	s_addc_u32 s37, s35, 0
	s_mov_b32 s65, m0
	s_mov_b32 m0, s48
	s_nop 3
	global_load_lds_dwordx4 v162, s[36:37]
	s_mov_b32 m0, s65
	s_nop 0
	s_mov_b32 s65, m0
	s_mov_b32 m0, s49
	s_nop 3
	global_load_lds_dwordx4 v164, s[36:37]
	s_mov_b32 m0, s65
	s_mov_b32 s36, m0
	s_mov_b32 m0, s44
	s_nop 3
	global_load_lds_dwordx4 v0, s[38:39]
	s_mov_b32 m0, s36
	s_nop 0
	s_mov_b32 s36, m0
	s_mov_b32 m0, s50
	s_nop 3
	global_load_lds_dwordx4 v163, s[38:39]
	s_mov_b32 m0, s36
	s_waitcnt vmcnt(8)
	s_waitcnt lgkmcnt(0)
	s_barrier
	s_waitcnt lgkmcnt(6)
	v_mfma_scale_f32_16x16x128_f8f6f4 v[90:93], v[26:33], v[172:179], v[90:93], v165, v166 op_sel_hi:[0,0,0]
	v_mfma_scale_f32_16x16x128_f8f6f4 v[94:97], v[18:25], v[172:179], v[94:97], v165, v166 op_sel_hi:[0,0,0]
	s_waitcnt lgkmcnt(4)
	v_mfma_scale_f32_16x16x128_f8f6f4 v[66:69], v[26:33], v[180:187], v[66:69], v165, v166 op_sel_hi:[0,0,0]
	v_mfma_scale_f32_16x16x128_f8f6f4 v[70:73], v[18:25], v[180:187], v[70:73], v165, v166 op_sel_hi:[0,0,0]
	s_waitcnt lgkmcnt(2)
	v_mfma_scale_f32_16x16x128_f8f6f4 v[50:53], v[26:33], v[188:195], v[50:53], v165, v166 op_sel_hi:[0,0,0]
	v_mfma_scale_f32_16x16x128_f8f6f4 v[54:57], v[18:25], v[188:195], v[54:57], v165, v166 op_sel_hi:[0,0,0]
	s_waitcnt lgkmcnt(0)
	v_mfma_scale_f32_16x16x128_f8f6f4 v[38:41], v[26:33], v[196:203], v[38:41], v165, v166 op_sel_hi:[0,0,0]
	v_mfma_scale_f32_16x16x128_f8f6f4 v[42:45], v[18:25], v[196:203], v[42:45], v165, v166 op_sel_hi:[0,0,0]
	v_mfma_scale_f32_16x16x128_f8f6f4 v[114:117], v[10:17], v[172:179], v[114:117], v165, v166 op_sel_hi:[0,0,0]
	v_mfma_scale_f32_16x16x128_f8f6f4 v[118:121], v[2:9], v[172:179], v[118:121], v165, v166 op_sel_hi:[0,0,0]
	v_mfma_scale_f32_16x16x128_f8f6f4 v[82:85], v[10:17], v[180:187], v[82:85], v165, v166 op_sel_hi:[0,0,0]
	v_mfma_scale_f32_16x16x128_f8f6f4 v[86:89], v[2:9], v[180:187], v[86:89], v165, v166 op_sel_hi:[0,0,0]
	v_mfma_scale_f32_16x16x128_f8f6f4 v[58:61], v[10:17], v[188:195], v[58:61], v165, v166 op_sel_hi:[0,0,0]
	v_mfma_scale_f32_16x16x128_f8f6f4 v[62:65], v[2:9], v[188:195], v[62:65], v165, v166 op_sel_hi:[0,0,0]
	v_mfma_scale_f32_16x16x128_f8f6f4 v[46:49], v[10:17], v[196:203], v[46:49], v165, v166 op_sel_hi:[0,0,0]
	v_mfma_scale_f32_16x16x128_f8f6f4 v[34:37], v[2:9], v[196:203], v[34:37], v165, v166 op_sel_hi:[0,0,0]
	s_barrier
	v_add_u32_e32 v2, 0x18000, v169
	v_add_u32_e32 v6, 0x1c000, v169
	ds_read_b128 v[26:29], v2
	ds_read_b128 v[30:33], v2 offset:1024
	ds_read_b128 v[18:21], v2 offset:2048
	ds_read_b128 v[22:25], v2 offset:3072
	ds_read_b128 v[10:13], v6
	ds_read_b128 v[14:17], v6 offset:1024
	ds_read_b128 v[2:5], v6 offset:2048
	ds_read_b128 v[6:9], v6 offset:3072
	ds_read_b128 v[172:175], v170 offset:32768
	ds_read_b128 v[176:179], v170 offset:33792
	ds_read_b128 v[180:183], v170 offset:34816
	ds_read_b128 v[184:187], v170 offset:35840
	ds_read_b128 v[188:191], v170 offset:36864
	ds_read_b128 v[192:195], v170 offset:37888
	ds_read_b128 v[196:199], v170 offset:38912
	ds_read_b128 v[200:203], v170 offset:39936
	s_add_u32 s36, s38, 0x20000
	s_addc_u32 s37, s39, 0
	s_mov_b32 s38, m0
	s_mov_b32 m0, s51
	s_nop 3
	global_load_lds_dwordx4 v0, s[36:37]
	s_mov_b32 m0, s38
	s_nop 0
	s_mov_b32 s38, m0
	s_mov_b32 m0, s52
	s_nop 3
	global_load_lds_dwordx4 v163, s[36:37]
	s_mov_b32 m0, s38
	s_waitcnt vmcnt(8)
	s_waitcnt lgkmcnt(0)
	s_barrier
	s_waitcnt lgkmcnt(6)
	v_mfma_scale_f32_16x16x128_f8f6f4 v[150:153], v[26:33], v[172:179], v[150:153], v165, v166 op_sel_hi:[0,0,0]
	v_mfma_scale_f32_16x16x128_f8f6f4 v[146:149], v[18:25], v[172:179], v[146:149], v165, v166 op_sel_hi:[0,0,0]
	s_waitcnt lgkmcnt(4)
	v_mfma_scale_f32_16x16x128_f8f6f4 v[130:133], v[26:33], v[180:187], v[130:133], v165, v166 op_sel_hi:[0,0,0]
	v_mfma_scale_f32_16x16x128_f8f6f4 v[134:137], v[18:25], v[180:187], v[134:137], v165, v166 op_sel_hi:[0,0,0]
	s_waitcnt lgkmcnt(2)
	v_mfma_scale_f32_16x16x128_f8f6f4 v[106:109], v[26:33], v[188:195], v[106:109], v165, v166 op_sel_hi:[0,0,0]
	v_mfma_scale_f32_16x16x128_f8f6f4 v[110:113], v[18:25], v[188:195], v[110:113], v165, v166 op_sel_hi:[0,0,0]
	s_waitcnt lgkmcnt(0)
	v_mfma_scale_f32_16x16x128_f8f6f4 v[74:77], v[26:33], v[196:203], v[74:77], v165, v166 op_sel_hi:[0,0,0]
	v_mfma_scale_f32_16x16x128_f8f6f4 v[78:81], v[18:25], v[196:203], v[78:81], v165, v166 op_sel_hi:[0,0,0]
	v_mfma_scale_f32_16x16x128_f8f6f4 v[158:161], v[10:17], v[172:179], v[158:161], v165, v166 op_sel_hi:[0,0,0]
	v_mfma_scale_f32_16x16x128_f8f6f4 v[154:157], v[2:9], v[172:179], v[154:157], v165, v166 op_sel_hi:[0,0,0]
	v_mfma_scale_f32_16x16x128_f8f6f4 v[138:141], v[10:17], v[180:187], v[138:141], v165, v166 op_sel_hi:[0,0,0]
	v_mfma_scale_f32_16x16x128_f8f6f4 v[142:145], v[2:9], v[180:187], v[142:145], v165, v166 op_sel_hi:[0,0,0]
	v_mfma_scale_f32_16x16x128_f8f6f4 v[122:125], v[10:17], v[188:195], v[122:125], v165, v166 op_sel_hi:[0,0,0]
	v_mfma_scale_f32_16x16x128_f8f6f4 v[126:129], v[2:9], v[188:195], v[126:129], v165, v166 op_sel_hi:[0,0,0]
	v_mfma_scale_f32_16x16x128_f8f6f4 v[98:101], v[10:17], v[196:203], v[98:101], v165, v166 op_sel_hi:[0,0,0]
	v_mfma_scale_f32_16x16x128_f8f6f4 v[102:105], v[2:9], v[196:203], v[102:105], v165, v166 op_sel_hi:[0,0,0]
	s_barrier
	ds_read_b128 v[172:175], v170 offset:49152
	ds_read_b128 v[176:179], v170 offset:50176
	ds_read_b128 v[180:183], v170 offset:51200
	ds_read_b128 v[184:187], v170 offset:52224
	ds_read_b128 v[188:191], v170 offset:53248
	ds_read_b128 v[192:195], v170 offset:54272
	ds_read_b128 v[196:199], v170 offset:55296
	ds_read_b128 v[200:203], v170 offset:56320
	s_add_u32 s36, s34, 0x80
	s_addc_u32 s37, s35, 0
	s_mov_b32 s38, m0
	s_mov_b32 m0, s14
	s_nop 3
	global_load_lds_dwordx4 v162, s[36:37]
	s_mov_b32 m0, s38
	s_add_u32 s34, s34, 0x20080
	s_mov_b32 s38, m0
	s_mov_b32 m0, s53
	s_nop 3
	global_load_lds_dwordx4 v164, s[36:37]
	s_mov_b32 m0, s38
	s_addc_u32 s35, s35, 0
	s_mov_b32 s36, m0
	s_mov_b32 m0, s56
	s_nop 3
	global_load_lds_dwordx4 v162, s[34:35]
	s_mov_b32 m0, s36
	s_nop 0
	s_mov_b32 s36, m0
	s_mov_b32 m0, s57
	s_nop 3
	global_load_lds_dwordx4 v164, s[34:35]
	s_mov_b32 m0, s36
	s_mov_b32 s34, m0
	s_mov_b32 m0, s54
	s_nop 3
	global_load_lds_dwordx4 v0, s[30:31]
	s_mov_b32 m0, s34
	s_nop 0
	s_mov_b32 s34, m0
	s_mov_b32 m0, s55
	s_nop 3
	global_load_lds_dwordx4 v163, s[30:31]
	s_mov_b32 m0, s34
	s_waitcnt vmcnt(8)
	s_waitcnt lgkmcnt(0)
	s_barrier
	s_waitcnt lgkmcnt(6)
	v_mfma_scale_f32_16x16x128_f8f6f4 v[90:93], v[26:33], v[172:179], v[90:93], v165, v166 op_sel_hi:[0,0,0]
	v_mfma_scale_f32_16x16x128_f8f6f4 v[94:97], v[18:25], v[172:179], v[94:97], v165, v166 op_sel_hi:[0,0,0]
	s_waitcnt lgkmcnt(4)
	v_mfma_scale_f32_16x16x128_f8f6f4 v[66:69], v[26:33], v[180:187], v[66:69], v165, v166 op_sel_hi:[0,0,0]
	v_mfma_scale_f32_16x16x128_f8f6f4 v[70:73], v[18:25], v[180:187], v[70:73], v165, v166 op_sel_hi:[0,0,0]
	s_waitcnt lgkmcnt(2)
	v_mfma_scale_f32_16x16x128_f8f6f4 v[50:53], v[26:33], v[188:195], v[50:53], v165, v166 op_sel_hi:[0,0,0]
	v_mfma_scale_f32_16x16x128_f8f6f4 v[54:57], v[18:25], v[188:195], v[54:57], v165, v166 op_sel_hi:[0,0,0]
	s_waitcnt lgkmcnt(0)
	v_mfma_scale_f32_16x16x128_f8f6f4 v[38:41], v[26:33], v[196:203], v[38:41], v165, v166 op_sel_hi:[0,0,0]
	v_mfma_scale_f32_16x16x128_f8f6f4 v[42:45], v[18:25], v[196:203], v[42:45], v165, v166 op_sel_hi:[0,0,0]
	v_mfma_scale_f32_16x16x128_f8f6f4 v[114:117], v[10:17], v[172:179], v[114:117], v165, v166 op_sel_hi:[0,0,0]
	v_mfma_scale_f32_16x16x128_f8f6f4 v[118:121], v[2:9], v[172:179], v[118:121], v165, v166 op_sel_hi:[0,0,0]
	v_mfma_scale_f32_16x16x128_f8f6f4 v[82:85], v[10:17], v[180:187], v[82:85], v165, v166 op_sel_hi:[0,0,0]
	v_mfma_scale_f32_16x16x128_f8f6f4 v[86:89], v[2:9], v[180:187], v[86:89], v165, v166 op_sel_hi:[0,0,0]
	v_mfma_scale_f32_16x16x128_f8f6f4 v[58:61], v[10:17], v[188:195], v[58:61], v165, v166 op_sel_hi:[0,0,0]
	v_mfma_scale_f32_16x16x128_f8f6f4 v[62:65], v[2:9], v[188:195], v[62:65], v165, v166 op_sel_hi:[0,0,0]
	v_mfma_scale_f32_16x16x128_f8f6f4 v[46:49], v[10:17], v[196:203], v[46:49], v165, v166 op_sel_hi:[0,0,0]
	v_mfma_scale_f32_16x16x128_f8f6f4 v[34:37], v[2:9], v[196:203], v[34:37], v165, v166 op_sel_hi:[0,0,0]
	s_barrier
	s_add_i32 s64, s64, 2
	s_add_u32 s62, s62, 0x100
	s_addc_u32 s63, s63, 0
	s_cmp_gt_u32 s64, 5
	s_mov_b64 s[36:37], s[28:29]
	s_cbranch_scc0 .LBB0_1323
	s_and_b64 vcc, exec, s[12:13]
	s_cbranch_vccz .LBB0_1326
	s_barrier

.LBB0_1337:
	s_setprio 0
	s_waitcnt vmcnt(0)
	v_readlane_b32 s54, v253, 31
	v_readlane_b32 s48, v253, 33
	v_readlane_b32 s50, v253, 35
	v_readlane_b32 s44, v253, 43
	v_readlane_b32 s24, v253, 45
	v_readlane_b32 s55, v253, 32
	v_readlane_b32 s49, v253, 34
	v_readlane_b32 s51, v253, 36
	v_readlane_b32 s45, v253, 44
	v_readlane_b32 s25, v253, 46
	s_movk_i32 s43, 0x4000
	v_readlane_b32 s47, v253, 50
	s_mov_b32 s56, s88
	s_barrier
